# v55 + RG-LRU phases: one static s_setprio 1 for waves 0-3 (the forward half), reset at phase end
# baseline (speedup 1.0000x reference)
; #define LAS __attribute__((address_space(3)))
; template <bool FINAL> __device__ __forceinline__ void rglru_pass(Frame& F) {
;     const bf16* Z1 = WSP(const bf16, WS_Z); const bf16* WGT = WSP(const bf16, WS_WGT); bf16* AO = WSP(bf16, WS_AO);
;     float* SUM = WSP(float, WS_SUM);
;     const float* cw = F.in[20]; const float* cb = F.in[21];
;     LAS unsigned char* XCB = F.lds;
;     LAS float* XCF = (LAS float*)(F.lds + 17408);
;     LAS float* HS = (LAS float*)(F.lds + 17408 + 32768);
;     const int bx = blockIdx.x, h = bx & 15, cg = bx >> 4, ncg = F.G >> 4;
;     if (cg >= ncg) return;
;     const int r = F.lane & 31, hh = F.lane >> 5, jg = F.wave & 3, z = F.wave >> 2;
;     const int chl = 32 * jg + r, ch = h * 128 + chl;
.LBB0_1351:
	s_cmp_ge_u32 s94, 4
	s_cbranch_scc1 .Lprio_rg0
	s_setprio 1
